# v036-histogram-reduction-pipelined-in-16-row-batches
# speedup vs baseline: 1.0099x; 1.0027x over previous
.LBB1_20:
	s_or_b64 exec, exec, s[4:5]
	v_and_b32_e32 v10, 0x7f, v0
	s_movk_i32 s3, 0x31
	v_cmp_gt_u32_e32 vcc, s3, v10
	s_and_saveexec_b64 s[6:7], vcc
	s_cbranch_execz .LBB1_22
	s_load_dwordx2 s[4:5], s[0:1], 0x18
	v_lshrrev_b32_e32 v25, 7, v0
	v_lshlrev_b32_e32 v29, 5, v10
	v_lshlrev_b32_e32 v28, 4, v10
	s_movk_i32 s3, 0x620
	v_readfirstlane_b32 s12, v0
	v_mad_u32_u24 v25, v25, s3, v29
	s_lshr_b32 s12, s12, 7
	s_lshl_b32 s13, s12, 6
	s_mul_i32 s14, s13, 0x310
	s_sub_i32 s15, s2, s13
	v_mov_b32_e32 v30, 0
	v_mov_b32_e32 v31, 0
	v_mov_b32_e32 v32, 0
	v_mov_b32_e32 v33, 0
	v_mov_b32_e32 v34, 0
	v_mov_b32_e32 v35, 0
	v_mov_b32_e32 v36, 0
	v_mov_b32_e32 v37, 0
	v_mov_b32_e32 v38, 0
	v_mov_b32_e32 v39, 0
	v_mov_b32_e32 v40, 0
	v_mov_b32_e32 v41, 0
	v_mov_b32_e32 v42, 0
	v_mov_b32_e32 v43, 0
	v_mov_b32_e32 v44, 0
	v_mov_b32_e32 v45, 0
	s_waitcnt lgkmcnt(0)
	s_add_u32 s4, s4, s14
	s_addc_u32 s5, s5, 0
	global_load_dwordx4 v[68:71], v28, s[4:5]
	global_load_dwordx4 v[72:75], v28, s[4:5] offset:784
	global_load_dwordx4 v[76:79], v28, s[4:5] offset:1568
	global_load_dwordx4 v[80:83], v28, s[4:5] offset:2352
	global_load_dwordx4 v[84:87], v28, s[4:5] offset:3136
	s_add_u32 s4, s4, 0xf50
	s_addc_u32 s5, s5, 0
	global_load_dwordx4 v[88:91], v28, s[4:5]
	global_load_dwordx4 v[92:95], v28, s[4:5] offset:784
	global_load_dwordx4 v[96:99], v28, s[4:5] offset:1568
	global_load_dwordx4 v[100:103], v28, s[4:5] offset:2352
	global_load_dwordx4 v[104:107], v28, s[4:5] offset:3136
	s_add_u32 s4, s4, 0xf50
	s_addc_u32 s5, s5, 0
	global_load_dwordx4 v[108:111], v28, s[4:5]
	global_load_dwordx4 v[112:115], v28, s[4:5] offset:784
	global_load_dwordx4 v[116:119], v28, s[4:5] offset:1568
	global_load_dwordx4 v[120:123], v28, s[4:5] offset:2352
	global_load_dwordx4 v[124:127], v28, s[4:5] offset:3136
	s_add_u32 s4, s4, 0xf50
	s_addc_u32 s5, s5, 0
	global_load_dwordx4 v[128:131], v28, s[4:5]
	global_load_dwordx4 v[132:135], v28, s[4:5] offset:784
	global_load_dwordx4 v[136:139], v28, s[4:5] offset:1568
	global_load_dwordx4 v[140:143], v28, s[4:5] offset:2352
	global_load_dwordx4 v[144:147], v28, s[4:5] offset:3136
	s_add_u32 s4, s4, 0xf50
	s_addc_u32 s5, s5, 0
	global_load_dwordx4 v[148:151], v28, s[4:5]
	global_load_dwordx4 v[152:155], v28, s[4:5] offset:784
	global_load_dwordx4 v[156:159], v28, s[4:5] offset:1568
	global_load_dwordx4 v[160:163], v28, s[4:5] offset:2352
	global_load_dwordx4 v[164:167], v28, s[4:5] offset:3136
	s_add_u32 s4, s4, 0xf50
	s_addc_u32 s5, s5, 0
	global_load_dwordx4 v[168:171], v28, s[4:5]
	global_load_dwordx4 v[172:175], v28, s[4:5] offset:784
	global_load_dwordx4 v[176:179], v28, s[4:5] offset:1568
	global_load_dwordx4 v[180:183], v28, s[4:5] offset:2352
	global_load_dwordx4 v[184:187], v28, s[4:5] offset:3136
	s_add_u32 s4, s4, 0xf50
	s_addc_u32 s5, s5, 0
	global_load_dwordx4 v[188:191], v28, s[4:5]
	global_load_dwordx4 v[192:195], v28, s[4:5] offset:784
	s_waitcnt vmcnt(16)
	v_add3_u32 v46, v68, v72, v76
	v_add3_u32 v46, v46, v80, v84
	v_add3_u32 v46, v46, v88, v92
	v_add3_u32 v46, v46, v96, v100
	v_add3_u32 v46, v46, v104, v108
	v_add3_u32 v46, v46, v112, v116
	v_add3_u32 v46, v46, v120, v124
	v_add_u32_e32 v46, v46, v128
	v_add3_u32 v47, v69, v73, v77
	v_add3_u32 v47, v47, v81, v85
	v_add3_u32 v47, v47, v89, v93
	v_add3_u32 v47, v47, v97, v101
	v_add3_u32 v47, v47, v105, v109
	v_add3_u32 v47, v47, v113, v117
	v_add3_u32 v47, v47, v121, v125
	v_add_u32_e32 v47, v47, v129
	v_add3_u32 v48, v70, v74, v78
	v_add3_u32 v48, v48, v82, v86
	v_add3_u32 v48, v48, v90, v94
	v_add3_u32 v48, v48, v98, v102
	v_add3_u32 v48, v48, v106, v110
	v_add3_u32 v48, v48, v114, v118
	v_add3_u32 v48, v48, v122, v126
	v_add_u32_e32 v48, v48, v130
	v_add3_u32 v49, v71, v75, v79
	v_add3_u32 v49, v49, v83, v87
	v_add3_u32 v49, v49, v91, v95
	v_add3_u32 v49, v49, v99, v103
	v_add3_u32 v49, v49, v107, v111
	v_add3_u32 v49, v49, v115, v119
	v_add3_u32 v49, v49, v123, v127
	v_add_u32_e32 v49, v49, v131
	v_and_b32_e32 v50, 0xffff, v46
	v_lshrrev_b32_e32 v51, 16, v46
	v_and_b32_e32 v52, 0xffff, v47
	v_lshrrev_b32_e32 v53, 16, v47
	v_and_b32_e32 v54, 0xffff, v48
	v_lshrrev_b32_e32 v55, 16, v48
	v_and_b32_e32 v56, 0xffff, v49
	v_lshrrev_b32_e32 v57, 16, v49
	v_add_u32_e32 v30, v30, v50
	v_add_u32_e32 v31, v31, v51
	v_add_u32_e32 v32, v32, v52
	v_add_u32_e32 v33, v33, v53
	v_add_u32_e32 v34, v34, v54
	v_add_u32_e32 v35, v35, v55
	v_add_u32_e32 v36, v36, v56
	v_add_u32_e32 v37, v37, v57
	s_cmp_ge_i32 s15, 16
	s_cbranch_scc0 .Lbscat_nf_0
	v_add_u32_e32 v38, v38, v50
	v_add_u32_e32 v39, v39, v51
	v_add_u32_e32 v40, v40, v52
	v_add_u32_e32 v41, v41, v53
	v_add_u32_e32 v42, v42, v54
	v_add_u32_e32 v43, v43, v55
	v_add_u32_e32 v44, v44, v56
	v_add_u32_e32 v45, v45, v57
	s_branch .Lbscat_dn_0

.Lbscat_dn_0:
	global_load_dwordx4 v[68:71], v28, s[4:5] offset:1568
	global_load_dwordx4 v[72:75], v28, s[4:5] offset:2352
	global_load_dwordx4 v[76:79], v28, s[4:5] offset:3136
	s_add_u32 s4, s4, 0xf50
	s_addc_u32 s5, s5, 0
	global_load_dwordx4 v[80:83], v28, s[4:5]
	global_load_dwordx4 v[84:87], v28, s[4:5] offset:784
	global_load_dwordx4 v[88:91], v28, s[4:5] offset:1568
	global_load_dwordx4 v[92:95], v28, s[4:5] offset:2352
	global_load_dwordx4 v[96:99], v28, s[4:5] offset:3136
	s_add_u32 s4, s4, 0xf50
	s_addc_u32 s5, s5, 0
	global_load_dwordx4 v[100:103], v28, s[4:5]
	global_load_dwordx4 v[104:107], v28, s[4:5] offset:784
	global_load_dwordx4 v[108:111], v28, s[4:5] offset:1568
	global_load_dwordx4 v[112:115], v28, s[4:5] offset:2352
	global_load_dwordx4 v[116:119], v28, s[4:5] offset:3136
	s_add_u32 s4, s4, 0xf50
	s_addc_u32 s5, s5, 0
	global_load_dwordx4 v[120:123], v28, s[4:5]
	global_load_dwordx4 v[124:127], v28, s[4:5] offset:784
	global_load_dwordx4 v[128:131], v28, s[4:5] offset:1568
	s_waitcnt vmcnt(16)
	v_add3_u32 v46, v132, v136, v140
	v_add3_u32 v46, v46, v144, v148
	v_add3_u32 v46, v46, v152, v156
	v_add3_u32 v46, v46, v160, v164
	v_add3_u32 v46, v46, v168, v172
	v_add3_u32 v46, v46, v176, v180
	v_add3_u32 v46, v46, v184, v188
	v_add_u32_e32 v46, v46, v192
	v_add3_u32 v47, v133, v137, v141
	v_add3_u32 v47, v47, v145, v149
	v_add3_u32 v47, v47, v153, v157
	v_add3_u32 v47, v47, v161, v165
	v_add3_u32 v47, v47, v169, v173
	v_add3_u32 v47, v47, v177, v181
	v_add3_u32 v47, v47, v185, v189
	v_add_u32_e32 v47, v47, v193
	v_add3_u32 v48, v134, v138, v142
	v_add3_u32 v48, v48, v146, v150
	v_add3_u32 v48, v48, v154, v158
	v_add3_u32 v48, v48, v162, v166
	v_add3_u32 v48, v48, v170, v174
	v_add3_u32 v48, v48, v178, v182
	v_add3_u32 v48, v48, v186, v190
	v_add_u32_e32 v48, v48, v194
	v_add3_u32 v49, v135, v139, v143
	v_add3_u32 v49, v49, v147, v151
	v_add3_u32 v49, v49, v155, v159
	v_add3_u32 v49, v49, v163, v167
	v_add3_u32 v49, v49, v171, v175
	v_add3_u32 v49, v49, v179, v183
	v_add3_u32 v49, v49, v187, v191
	v_add_u32_e32 v49, v49, v195
	v_and_b32_e32 v50, 0xffff, v46
	v_lshrrev_b32_e32 v51, 16, v46
	v_and_b32_e32 v52, 0xffff, v47
	v_lshrrev_b32_e32 v53, 16, v47
	v_and_b32_e32 v54, 0xffff, v48
	v_lshrrev_b32_e32 v55, 16, v48
	v_and_b32_e32 v56, 0xffff, v49
	v_lshrrev_b32_e32 v57, 16, v49
	v_add_u32_e32 v30, v30, v50
	v_add_u32_e32 v31, v31, v51
	v_add_u32_e32 v32, v32, v52
	v_add_u32_e32 v33, v33, v53
	v_add_u32_e32 v34, v34, v54
	v_add_u32_e32 v35, v35, v55
	v_add_u32_e32 v36, v36, v56
	v_add_u32_e32 v37, v37, v57
	s_cmp_ge_i32 s15, 32
	s_cbranch_scc0 .Lbscat_nf_1
	v_add_u32_e32 v38, v38, v50
	v_add_u32_e32 v39, v39, v51
	v_add_u32_e32 v40, v40, v52
	v_add_u32_e32 v41, v41, v53
	v_add_u32_e32 v42, v42, v54
	v_add_u32_e32 v43, v43, v55
	v_add_u32_e32 v44, v44, v56
	v_add_u32_e32 v45, v45, v57
	s_branch .Lbscat_dn_1

.Lbscat_dn_1:
	global_load_dwordx4 v[132:135], v28, s[4:5] offset:2352
	global_load_dwordx4 v[136:139], v28, s[4:5] offset:3136
	s_add_u32 s4, s4, 0xf50
	s_addc_u32 s5, s5, 0
	global_load_dwordx4 v[140:143], v28, s[4:5]
	global_load_dwordx4 v[144:147], v28, s[4:5] offset:784
	global_load_dwordx4 v[148:151], v28, s[4:5] offset:1568
	global_load_dwordx4 v[152:155], v28, s[4:5] offset:2352
	global_load_dwordx4 v[156:159], v28, s[4:5] offset:3136
	s_add_u32 s4, s4, 0xf50
	s_addc_u32 s5, s5, 0
	global_load_dwordx4 v[160:163], v28, s[4:5]
	global_load_dwordx4 v[164:167], v28, s[4:5] offset:784
	global_load_dwordx4 v[168:171], v28, s[4:5] offset:1568
	global_load_dwordx4 v[172:175], v28, s[4:5] offset:2352
	global_load_dwordx4 v[176:179], v28, s[4:5] offset:3136
	s_add_u32 s4, s4, 0xf50
	s_addc_u32 s5, s5, 0
	global_load_dwordx4 v[180:183], v28, s[4:5]
	global_load_dwordx4 v[184:187], v28, s[4:5] offset:784
	global_load_dwordx4 v[188:191], v28, s[4:5] offset:1568
	global_load_dwordx4 v[192:195], v28, s[4:5] offset:2352
	s_waitcnt vmcnt(16)
	v_add3_u32 v46, v68, v72, v76
	v_add3_u32 v46, v46, v80, v84
	v_add3_u32 v46, v46, v88, v92
	v_add3_u32 v46, v46, v96, v100
	v_add3_u32 v46, v46, v104, v108
	v_add3_u32 v46, v46, v112, v116
	v_add3_u32 v46, v46, v120, v124
	v_add_u32_e32 v46, v46, v128
	v_add3_u32 v47, v69, v73, v77
	v_add3_u32 v47, v47, v81, v85
	v_add3_u32 v47, v47, v89, v93
	v_add3_u32 v47, v47, v97, v101
	v_add3_u32 v47, v47, v105, v109
	v_add3_u32 v47, v47, v113, v117
	v_add3_u32 v47, v47, v121, v125
	v_add_u32_e32 v47, v47, v129
	v_add3_u32 v48, v70, v74, v78
	v_add3_u32 v48, v48, v82, v86
	v_add3_u32 v48, v48, v90, v94
	v_add3_u32 v48, v48, v98, v102
	v_add3_u32 v48, v48, v106, v110
	v_add3_u32 v48, v48, v114, v118
	v_add3_u32 v48, v48, v122, v126
	v_add_u32_e32 v48, v48, v130
	v_add3_u32 v49, v71, v75, v79
	v_add3_u32 v49, v49, v83, v87
	v_add3_u32 v49, v49, v91, v95
	v_add3_u32 v49, v49, v99, v103
	v_add3_u32 v49, v49, v107, v111
	v_add3_u32 v49, v49, v115, v119
	v_add3_u32 v49, v49, v123, v127
	v_add_u32_e32 v49, v49, v131
	v_and_b32_e32 v50, 0xffff, v46
	v_lshrrev_b32_e32 v51, 16, v46
	v_and_b32_e32 v52, 0xffff, v47
	v_lshrrev_b32_e32 v53, 16, v47
	v_and_b32_e32 v54, 0xffff, v48
	v_lshrrev_b32_e32 v55, 16, v48
	v_and_b32_e32 v56, 0xffff, v49
	v_lshrrev_b32_e32 v57, 16, v49
	v_add_u32_e32 v30, v30, v50
	v_add_u32_e32 v31, v31, v51
	v_add_u32_e32 v32, v32, v52
	v_add_u32_e32 v33, v33, v53
	v_add_u32_e32 v34, v34, v54
	v_add_u32_e32 v35, v35, v55
	v_add_u32_e32 v36, v36, v56
	v_add_u32_e32 v37, v37, v57
	s_cmp_ge_i32 s15, 48
	s_cbranch_scc0 .Lbscat_nf_2
	v_add_u32_e32 v38, v38, v50
	v_add_u32_e32 v39, v39, v51
	v_add_u32_e32 v40, v40, v52
	v_add_u32_e32 v41, v41, v53
	v_add_u32_e32 v42, v42, v54
	v_add_u32_e32 v43, v43, v55
	v_add_u32_e32 v44, v44, v56
	v_add_u32_e32 v45, v45, v57
	s_branch .Lbscat_dn_2

.Lbscat_dn_2:
	s_waitcnt vmcnt(0)
	v_add3_u32 v46, v132, v136, v140
	v_add3_u32 v46, v46, v144, v148
	v_add3_u32 v46, v46, v152, v156
	v_add3_u32 v46, v46, v160, v164
	v_add3_u32 v46, v46, v168, v172
	v_add3_u32 v46, v46, v176, v180
	v_add3_u32 v46, v46, v184, v188
	v_add_u32_e32 v46, v46, v192
	v_add3_u32 v47, v133, v137, v141
	v_add3_u32 v47, v47, v145, v149
	v_add3_u32 v47, v47, v153, v157
	v_add3_u32 v47, v47, v161, v165
	v_add3_u32 v47, v47, v169, v173
	v_add3_u32 v47, v47, v177, v181
	v_add3_u32 v47, v47, v185, v189
	v_add_u32_e32 v47, v47, v193
	v_add3_u32 v48, v134, v138, v142
	v_add3_u32 v48, v48, v146, v150
	v_add3_u32 v48, v48, v154, v158
	v_add3_u32 v48, v48, v162, v166
	v_add3_u32 v48, v48, v170, v174
	v_add3_u32 v48, v48, v178, v182
	v_add3_u32 v48, v48, v186, v190
	v_add_u32_e32 v48, v48, v194
	v_add3_u32 v49, v135, v139, v143
	v_add3_u32 v49, v49, v147, v151
	v_add3_u32 v49, v49, v155, v159
	v_add3_u32 v49, v49, v163, v167
	v_add3_u32 v49, v49, v171, v175
	v_add3_u32 v49, v49, v179, v183
	v_add3_u32 v49, v49, v187, v191
	v_add_u32_e32 v49, v49, v195
	v_and_b32_e32 v50, 0xffff, v46
	v_lshrrev_b32_e32 v51, 16, v46
	v_and_b32_e32 v52, 0xffff, v47
	v_lshrrev_b32_e32 v53, 16, v47
	v_and_b32_e32 v54, 0xffff, v48
	v_lshrrev_b32_e32 v55, 16, v48
	v_and_b32_e32 v56, 0xffff, v49
	v_lshrrev_b32_e32 v57, 16, v49
	v_add_u32_e32 v30, v30, v50
	v_add_u32_e32 v31, v31, v51
	v_add_u32_e32 v32, v32, v52
	v_add_u32_e32 v33, v33, v53
	v_add_u32_e32 v34, v34, v54
	v_add_u32_e32 v35, v35, v55
	v_add_u32_e32 v36, v36, v56
	v_add_u32_e32 v37, v37, v57
	s_cmp_ge_i32 s15, 64
	s_cbranch_scc0 .Lbscat_nf_3
	v_add_u32_e32 v38, v38, v50
	v_add_u32_e32 v39, v39, v51
	v_add_u32_e32 v40, v40, v52
	v_add_u32_e32 v41, v41, v53
	v_add_u32_e32 v42, v42, v54
	v_add_u32_e32 v43, v43, v55
	v_add_u32_e32 v44, v44, v56
	v_add_u32_e32 v45, v45, v57
	s_branch .Lbscat_dn_3
